# v23 + HGRN2 chunk-loop header: counted vmcnt raised by 4 so the header no longer waits for the previous chunk's output-store acknowledgements (4 dummy loads equalise the first chunk)
# speedup vs baseline: 1.0125x; 1.0044x over previous
.LBB0_354:
	v_add_u32_e32 v8, 0x200, v8
	s_movk_i32 s70, 0x1fff
	v_cmp_lt_u32_e32 vcc, s70, v8
	ds_write_b32 v7, v69
	s_or_b64 s[58:59], vcc, s[58:59]
	v_add_u32_e32 v7, 0x800, v7
	s_andn2_b64 exec, exec, s[58:59]
	s_cbranch_execnz .LBB0_354
	s_or_b64 exec, exec, s[58:59]
	s_waitcnt vmcnt(0)
	v_sub_f32_e32 v4, v4, v2
	v_mul_f32_e32 v2, 0x3fb8aa3b, v4
	s_mov_b32 s46, 0x3fb8aa3b
	v_fma_f32 v7, v4, s46, -v2
	v_rndne_f32_e32 v8, v2
	v_fmac_f32_e32 v7, 0x32a5705f, v4
	v_sub_f32_e32 v2, v2, v8
	v_add_f32_e32 v2, v2, v7
	v_cvt_i32_f32_e32 v7, v8
	v_exp_f32_e32 v2, v2
	v_sub_f32_e32 v3, v5, v3
	s_and_b64 s[58:59], s[40:41], exec
	v_readlane_b32 s58, v254, 15
	v_ldexp_f32 v7, v2, v7
	v_mul_f32_e32 v2, 0x3fb8aa3b, v3
	v_fma_f32 v5, v3, s46, -v2
	v_rndne_f32_e32 v8, v2
	v_fmac_f32_e32 v5, 0x32a5705f, v3
	v_sub_f32_e32 v2, v2, v8
	v_add_f32_e32 v2, v2, v5
	v_exp_f32_e32 v5, v2
	v_cvt_i32_f32_e32 v8, v8
	s_mov_b32 s46, 0xc2ce8ed0
	v_cmp_ngt_f32_e32 vcc, s46, v4
	s_mov_b32 s89, 0x42b17218
	v_ldexp_f32 v5, v5, v8
	v_cndmask_b32_e32 v7, 0, v7, vcc
	v_cmp_ngt_f32_e32 vcc, s46, v3
	v_readlane_b32 s46, v254, 26
	s_cselect_b32 s58, s58, s46
	v_cndmask_b32_e32 v5, 0, v5, vcc
	v_cmp_nlt_f32_e32 vcc, s89, v3
	s_mulk_i32 s58, 0x1c00
	v_readlane_b32 s46, v254, 27
	v_cndmask_b32_e32 v3, v215, v5, vcc
	v_or_b32_e32 v5, s58, v6
	s_cselect_b32 s58, s60, s46
	s_mulk_i32 s58, 0x1c00
	v_readlane_b32 s46, v254, 28
	v_readlane_b32 s47, v254, 29
	v_or_b32_e32 v8, s58, v6
	s_cselect_b32 s58, s46, s47
	s_mulk_i32 s58, 0x1c00
	v_readlane_b32 s46, v254, 30
	v_readlane_b32 s47, v254, 31
	v_or_b32_e32 v9, s58, v6
	s_cselect_b32 s58, s46, s47
	s_mulk_i32 s58, 0x1c00
	v_readlane_b32 s46, v254, 32
	v_readlane_b32 s47, v254, 33
	v_or_b32_e32 v10, s58, v6
	s_cselect_b32 s58, s46, s47
	s_mulk_i32 s58, 0x1c00
	v_readlane_b32 s46, v254, 34
	v_readlane_b32 s47, v254, 35
	v_or_b32_e32 v11, s58, v6
	s_cselect_b32 s58, s46, s47
	s_mulk_i32 s58, 0x1c00
	v_readlane_b32 s46, v254, 36
	v_readlane_b32 s47, v254, 37
	v_or_b32_e32 v12, s58, v6
	s_cselect_b32 s58, s46, s47
	s_mulk_i32 s58, 0x1c00
	v_readlane_b32 s46, v254, 38
	v_readlane_b32 s47, v254, 39
	v_or_b32_e32 v13, s58, v6
	s_cselect_b32 s58, s46, s47
	s_mulk_i32 s58, 0x1c00
	v_add_f32_e32 v3, 1.0, v3
	v_or_b32_e32 v6, s58, v6
	v_lshlrev_b32_e32 v50, 1, v6
	v_div_scale_f32 v6, s[58:59], v3, v3, 1.0
	s_movk_i32 s58, 0x1800
	s_cselect_b32 s70, s58, 0x2000
	s_mov_b32 s58, 0x16600000
	s_cselect_b32 s58, s58, 0x1a600000
	s_add_u32 s82, s66, s58
	s_addc_u32 s83, s67, 0
	s_lshl_b32 s58, s5, 7
	s_and_b32 s88, s58, 0xfffff800
	s_and_b64 s[58:59], s[40:41], exec
	s_cselect_b32 s58, 0, 0x7c0
	s_or_b32 s58, s58, s88
	s_mul_hi_i32 s59, s58, 0x3800
	s_mulk_i32 s58, 0x3800
	s_add_u32 s86, s55, s58
	s_addc_u32 s87, s73, s59
	s_add_u32 s58, s86, s70
	s_addc_u32 s59, s87, 0
	s_add_u32 s84, s86, 0x1000
	s_addc_u32 s85, s87, 0
	v_lshlrev_b32_e32 v68, 1, v5
	s_add_u32 s86, s86, 0x2800
	v_lshlrev_b32_e32 v52, 1, v8
	v_lshlrev_b32_e32 v54, 1, v9
	v_lshlrev_b32_e32 v56, 1, v10
	v_lshlrev_b32_e32 v58, 1, v11
	v_lshlrev_b32_e32 v60, 1, v12
	v_lshlrev_b32_e32 v62, 1, v13
	s_addc_u32 s87, s87, 0
	global_load_dword v87, v68, s[58:59]
	global_load_dword v89, v68, s[84:85]
	global_load_dword v91, v68, s[86:87]
	global_load_dword v93, v52, s[58:59]
	global_load_dword v97, v52, s[84:85]
	global_load_dword v107, v52, s[86:87]
	global_load_dword v147, v54, s[84:85]
	global_load_dword v148, v54, s[86:87]
	global_load_dword v146, v54, s[58:59]
	global_load_dword v149, v56, s[58:59]
	global_load_dword v150, v56, s[84:85]
	global_load_dword v151, v56, s[86:87]
	global_load_dword v152, v58, s[58:59]
	global_load_dword v153, v58, s[84:85]
	global_load_dword v154, v58, s[86:87]
	global_load_dword v157, v60, s[86:87]
	global_load_dword v155, v60, s[58:59]
	global_load_dword v156, v60, s[84:85]
	global_load_dword v158, v62, s[58:59]
	global_load_dword v159, v62, s[84:85]
	global_load_dword v160, v62, s[86:87]
	global_load_dword v161, v50, s[58:59]
	global_load_dword v164, v50, s[84:85]
	global_load_dword v165, v50, s[86:87]
	global_load_dword v70, v50, s[86:87]
	global_load_dword v70, v50, s[86:87]
	global_load_dword v70, v50, s[86:87]
	global_load_dword v70, v50, s[86:87]
	v_rcp_f32_e32 v14, v6
	v_cmp_nlt_f32_e32 vcc, s89, v4
	v_readlane_b32 s46, v254, 40
	s_waitcnt lgkmcnt(0)
	v_fma_f32 v5, -v6, v14, 1.0
	v_cndmask_b32_e32 v4, v215, v7, vcc
	v_fmac_f32_e32 v14, v5, v14
	v_div_scale_f32 v5, vcc, 1.0, v3, 1.0
	v_mul_f32_e32 v7, v5, v14
	v_fma_f32 v8, -v6, v7, v5
	v_fmac_f32_e32 v7, v8, v14
	v_fma_f32 v5, -v6, v7, v5
	v_add_f32_e32 v4, 1.0, v4
	v_div_fmas_f32 v5, v5, v14, v7
	v_div_fixup_f32 v65, v5, v3, 1.0
	v_div_scale_f32 v3, s[58:59], v4, v4, 1.0
	v_rcp_f32_e32 v5, v3
	v_or_b32_e32 v6, s61, v189
	v_lshlrev_b32_e32 v6, 1, v6
	s_barrier
	v_fma_f32 v7, -v3, v5, 1.0
	v_fmac_f32_e32 v5, v7, v5
	v_div_scale_f32 v7, vcc, 1.0, v4, 1.0
	v_mul_f32_e32 v8, v7, v5
	v_fma_f32 v9, -v3, v8, v7
	v_fmac_f32_e32 v8, v9, v5
	v_fma_f32 v3, -v3, v8, v7
	v_div_fmas_f32 v3, v3, v5, v8
	v_div_fixup_f32 v64, v3, v4, 1.0
	v_cndmask_b32_e64 v3, v188, v187, s[40:41]
	v_lshlrev_b32_e32 v3, 11, v3
	v_mov_b32_e32 v2, 0
	v_or3_b32 v4, v6, s46, v3
	v_mov_b32_e32 v5, v69
	s_mov_b32 s89, 0
	v_pk_add_f32 v[108:109], v[64:65], 1.0 op_sel_hi:[1,0] neg_lo:[1,0] neg_hi:[1,0]
	v_mov_b32_e32 v53, v69
	v_mov_b32_e32 v55, v69
	v_mov_b32_e32 v57, v69
	v_mov_b32_e32 v59, v69
	v_mov_b32_e32 v61, v69
	v_mov_b32_e32 v63, v69
	v_mov_b32_e32 v51, v69
	v_lshl_add_u64 v[110:111], s[82:83], 0, v[4:5]
	s_movk_i32 s90, 0x780
	s_mov_b32 s91, 0
	v_mov_b32_e32 v3, v2
	v_mov_b32_e32 v4, v2
	v_mov_b32_e32 v5, v2
	v_mov_b32_e32 v6, v2
	v_mov_b32_e32 v7, v2
	v_mov_b32_e32 v8, v2
	v_mov_b32_e32 v9, v2
	v_mov_b32_e32 v10, v2
	v_mov_b32_e32 v11, v2
	v_mov_b32_e32 v12, v2
	v_mov_b32_e32 v13, v2
	v_mov_b32_e32 v14, v2
	v_mov_b32_e32 v15, v2
	v_mov_b32_e32 v16, v2
	v_mov_b32_e32 v17, v2
	v_mov_b32_e32 v18, v2
	v_mov_b32_e32 v19, v2
	v_mov_b32_e32 v20, v2
	v_mov_b32_e32 v21, v2
	v_mov_b32_e32 v22, v2
	v_mov_b32_e32 v23, v2
	v_mov_b32_e32 v24, v2
	v_mov_b32_e32 v25, v2
	v_mov_b32_e32 v26, v2
	v_mov_b32_e32 v27, v2
	v_mov_b32_e32 v28, v2
	v_mov_b32_e32 v29, v2
	v_mov_b32_e32 v30, v2
	v_mov_b32_e32 v31, v2
	v_mov_b32_e32 v32, v2
	v_mov_b32_e32 v33, v2
	s_branch .LBB0_357

.LBB0_357:
	s_waitcnt vmcnt(27)
	v_lshlrev_b32_e32 v34, 16, v87
	v_and_b32_e32 v35, 0xffff0000, v87
	v_mul_f32_e32 v34, 0xbfb8aa3b, v34
	v_mul_f32_e32 v35, 0xbfb8aa3b, v35
	v_exp_f32_e32 v34, v34
	v_exp_f32_e32 v35, v35
	s_waitcnt vmcnt(24)
	v_lshlrev_b32_e32 v36, 16, v93
	v_add_u32_e32 v167, 0, v190
	v_add_f32_e32 v34, 1.0, v34
	v_add_f32_e32 v35, 1.0, v35
	v_rcp_f32_e32 v34, v34
	v_rcp_f32_e32 v35, v35
	s_andn2_b64 vcc, exec, s[74:75]
	s_mov_b64 s[58:59], -1
	v_pk_mul_f32 v[120:121], v[108:109], v[34:35]
	v_and_b32_e32 v34, 0xffff0000, v93
	v_mul_f32_e32 v35, 0xbfb8aa3b, v36
	v_mul_f32_e32 v34, 0xbfb8aa3b, v34
	v_exp_f32_e32 v35, v35
	v_exp_f32_e32 v36, v34
	v_add_f32_e32 v37, v64, v120
	v_add_f32_e32 v38, v65, v121
	v_add_f32_e32 v34, 1.0, v35
	v_add_f32_e32 v35, 1.0, v36
	v_rcp_f32_e32 v34, v34
	v_rcp_f32_e32 v35, v35
	v_log_f32_e32 v36, v37
	v_log_f32_e32 v37, v38
	v_pk_mul_f32 v[122:123], v[108:109], v[34:35]
	s_waitcnt vmcnt(19)
	v_lshlrev_b32_e32 v34, 16, v146
	v_and_b32_e32 v35, 0xffff0000, v146
	v_mul_f32_e32 v34, 0xbfb8aa3b, v34
	v_mul_f32_e32 v35, 0xbfb8aa3b, v35
	v_exp_f32_e32 v34, v34
	v_exp_f32_e32 v35, v35
	v_add_f32_e32 v38, v64, v122
	v_add_f32_e32 v39, v65, v123
	v_add_f32_e32 v34, 1.0, v34
	v_add_f32_e32 v35, 1.0, v35
	v_rcp_f32_e32 v34, v34
	v_rcp_f32_e32 v35, v35
	v_log_f32_e32 v38, v38
	v_log_f32_e32 v39, v39
	v_pk_add_f32 v[144:145], v[36:37], 0 op_sel_hi:[1,0]
	v_pk_mul_f32 v[128:129], v[108:109], v[34:35]
	s_waitcnt vmcnt(18)
	v_lshlrev_b32_e32 v34, 16, v149
	v_and_b32_e32 v35, 0xffff0000, v149
	v_mul_f32_e32 v34, 0xbfb8aa3b, v34
	v_mul_f32_e32 v35, 0xbfb8aa3b, v35
	v_exp_f32_e32 v34, v34
	v_exp_f32_e32 v35, v35
	v_add_f32_e32 v40, v64, v128
	v_add_f32_e32 v41, v65, v129
	v_add_f32_e32 v34, 1.0, v34
	v_add_f32_e32 v35, 1.0, v35
	v_rcp_f32_e32 v34, v34
	v_rcp_f32_e32 v35, v35
	v_log_f32_e32 v40, v40
	v_log_f32_e32 v41, v41
	v_pk_add_f32 v[140:141], v[144:145], v[38:39]
	v_pk_mul_f32 v[126:127], v[108:109], v[34:35]
	s_waitcnt vmcnt(15)
	v_lshlrev_b32_e32 v34, 16, v152
	v_and_b32_e32 v35, 0xffff0000, v152
	v_mul_f32_e32 v34, 0xbfb8aa3b, v34
	v_mul_f32_e32 v35, 0xbfb8aa3b, v35
	v_exp_f32_e32 v34, v34
	v_exp_f32_e32 v35, v35
	v_add_f32_e32 v42, v64, v126
	v_add_f32_e32 v43, v65, v127
	v_add_f32_e32 v34, 1.0, v34
	v_add_f32_e32 v35, 1.0, v35
	v_rcp_f32_e32 v34, v34
	v_rcp_f32_e32 v35, v35
	v_log_f32_e32 v42, v42
	v_log_f32_e32 v43, v43
	v_pk_add_f32 v[136:137], v[140:141], v[40:41]
	v_pk_mul_f32 v[130:131], v[108:109], v[34:35]
	s_waitcnt vmcnt(11)
	v_lshlrev_b32_e32 v34, 16, v155
	v_and_b32_e32 v35, 0xffff0000, v155
	v_mul_f32_e32 v34, 0xbfb8aa3b, v34
	v_mul_f32_e32 v35, 0xbfb8aa3b, v35
	v_exp_f32_e32 v34, v34
	v_exp_f32_e32 v35, v35
	v_add_f32_e32 v44, v64, v130
	v_add_f32_e32 v45, v65, v131
	v_add_f32_e32 v34, 1.0, v34
	v_add_f32_e32 v35, 1.0, v35
	v_rcp_f32_e32 v34, v34
	v_rcp_f32_e32 v35, v35
	v_log_f32_e32 v44, v44
	v_log_f32_e32 v45, v45
	v_pk_add_f32 v[132:133], v[136:137], v[42:43]
	v_pk_mul_f32 v[134:135], v[108:109], v[34:35]
	s_waitcnt vmcnt(9)
	v_lshlrev_b32_e32 v34, 16, v158
	v_and_b32_e32 v35, 0xffff0000, v158
	v_mul_f32_e32 v34, 0xbfb8aa3b, v34
	v_mul_f32_e32 v35, 0xbfb8aa3b, v35
	v_exp_f32_e32 v34, v34
	v_exp_f32_e32 v35, v35
	v_add_f32_e32 v46, v64, v134
	v_add_f32_e32 v47, v65, v135
	v_add_f32_e32 v34, 1.0, v34
	v_add_f32_e32 v35, 1.0, v35
	v_rcp_f32_e32 v34, v34
	v_rcp_f32_e32 v35, v35
	v_log_f32_e32 v46, v46
	v_log_f32_e32 v47, v47
	v_pk_add_f32 v[124:125], v[132:133], v[44:45]
	v_pk_mul_f32 v[138:139], v[108:109], v[34:35]
	s_waitcnt vmcnt(6)
	v_lshlrev_b32_e32 v34, 16, v161
	v_and_b32_e32 v35, 0xffff0000, v161
	v_mul_f32_e32 v34, 0xbfb8aa3b, v34
	v_mul_f32_e32 v35, 0xbfb8aa3b, v35
	v_exp_f32_e32 v34, v34
	v_exp_f32_e32 v35, v35
	v_add_f32_e32 v48, v64, v138
	v_add_f32_e32 v49, v65, v139
	v_add_f32_e32 v34, 1.0, v34
	v_add_f32_e32 v35, 1.0, v35
	v_rcp_f32_e32 v34, v34
	v_rcp_f32_e32 v35, v35
	v_log_f32_e32 v48, v48
	v_log_f32_e32 v49, v49
	v_pk_add_f32 v[118:119], v[124:125], v[46:47]
	v_pk_mul_f32 v[142:143], v[108:109], v[34:35]
	v_and_b32_e32 v36, 0xffff, v154
	v_add_f32_e32 v34, v64, v142
	v_add_f32_e32 v35, v65, v143
	v_log_f32_e32 v34, v34
	v_log_f32_e32 v35, v35
	v_pk_add_f32 v[114:115], v[118:119], v[48:49]
	v_and_b32_e32 v37, 0xffff, v160
	v_lshl_or_b32 v36, v157, 16, v36
	v_pk_add_f32 v[112:113], v[114:115], v[34:35]
	v_add_u32_e32 v34, s63, v190
	ds_write_b64 v34, v[112:113]
	v_and_b32_e32 v34, 0xffff, v91
	v_and_b32_e32 v35, 0xffff, v148
	v_lshl_or_b32 v34, v107, 16, v34
	v_lshl_or_b32 v35, v151, 16, v35
	s_waitcnt vmcnt(4)
	v_lshl_or_b32 v37, v165, 16, v37
	v_lshrrev_b32_e32 v38, 16, v91
	v_lshrrev_b32_e32 v39, 16, v148
	v_lshrrev_b32_e32 v40, 16, v154
	v_lshrrev_b32_e32 v41, 16, v160
	v_add_u32_e32 v42, s64, v191
	v_and_or_b32 v38, v107, s53, v38
	v_and_or_b32 v39, v151, s53, v39
	v_and_or_b32 v40, v157, s53, v40
	v_and_or_b32 v41, v165, s53, v41
	ds_write_b128 v42, v[34:37] offset:53248
	ds_write_b128 v42, v[38:41] offset:53392
	s_waitcnt lgkmcnt(0)
	s_barrier
	v_add_u32_e32 v34, 0x24c00, v167
	ds_read2st64_b64 v[46:49], v34 offset1:1
	ds_read2st64_b64 v[42:45], v34 offset0:2 offset1:3
	ds_read2st64_b64 v[38:41], v34 offset0:4 offset1:5
	ds_read2st64_b64 v[34:37], v34 offset0:6 offset1:7
	s_waitcnt lgkmcnt(3)
	v_add_f32_e32 v166, 0, v46
	v_add_f32_e32 v46, v166, v48
	s_waitcnt lgkmcnt(2)
	v_add_f32_e32 v46, v46, v42
	v_add_f32_e32 v46, v46, v44
	s_waitcnt lgkmcnt(1)
	v_add_f32_e32 v46, v46, v38
	v_add_f32_e32 v46, v46, v40
	s_waitcnt lgkmcnt(0)
	v_add_f32_e32 v46, v46, v34
	v_add_f32_e32 v46, v46, v36
	v_exp_f32_e32 v116, v46
	s_cbranch_vccnz .LBB0_359
	s_mov_b64 s[58:59], 0
